# 416 (instead of 832) layer-1 expert-weight tiles converted in the in-projection slot
# speedup vs baseline: 1.0079x; 1.0016x over previous
; #define LAS __attribute__((address_space(3)))
; #define PH(k, ...) do { if (IN(pb + (k))) { { __VA_ARGS__ } if ((MK_DUP >> (k)) & 1) { xcd_barrier(bar); { __VA_ARGS__ } } } SEAM(pb + (k)); } while (0)
; DI void phase_p0(const Args& A, LAS unsigned char* lds, int it0, int it1, int gw, int ngw, int wave, int lane) {
;     ...
;     auto desc = [&](int item) { F8Tile d; const int r = item - I_IN - I_OUT; const int le = r / (3 * I_E), q = r % (3 * I_E), which = q / I_E, t = q % I_E;
;         if (which < 2) { const int kb = t / 44, nb = t % 44, n0 = nb * 64;
;             d.W = A.in[which == 0 ? I_EW1 : I_EW3] + (size_t)le * DM * FF; d.N = FF; d.k0 = kb * 128; d.n0 = n0; d.dst = w13 + (size_t)le * 5632 * DM; d.Kd = DM; d.drow0 = (size_t)((n0 >> 7) * 256 + which * 128 + (n0 & 127)); }
;         else { const int kb = t / 16, nb = t % 16;
;             d.W = A.in[I_EW2] + (size_t)le * FF * DM; d.N = DM; d.k0 = kb * 128; d.n0 = nb * 64; d.dst = w2t + (size_t)le * DM * FF; d.Kd = FF; d.drow0 = (size_t)nb * 64; }
;         return d; };
;     if (it < it1) {
;         f32x4 ra[4][4], rb[4][4]; LAS unsigned char* sc8 = (LAS unsigned char*)scr;
;         F8Tile d = desc(it);
;         f8_load(ra, d, 0, lane); f8_load(rb, d, 1, lane);
;         for (; it < it1; it += ngw) {
;             const bool vn = it + ngw < it1; F8Tile dn = d; if (vn) dn = desc(it + ngw);
; template <int l> DI void run_layer(const Args& A, LAS unsigned char* lds, const XcdBarrier& bar, int lo, int hi, int G, int bid, int tid, int lane, int wave, int gw, int ngw, int gtid, int nthr) {
;     ...
;     PH(1,
;         const bool conv = (l == 0) && (G >= 2 * P0_XC1) && (G % 8 == 0); const int Gg = conv ? G - P0_XC1 : G;
;         if (conv && bid >= Gg) { __syncthreads(); phase_p0(A, lds, P0_W, P0_SPLIT, (bid - Gg) * NWAVES + wave, P0_XC1 * NWAVES, wave, lane); __syncthreads(); }
;         else {
.LBB0_135:
	v_readlane_b32 s4, v235, 9
	v_readlane_b32 s6, v235, 11
	s_cmp_lt_i32 s6, 3
	v_readlane_b32 s7, v235, 12
	s_cselect_b64 s[0:1], -1, 0
	s_cmp_gt_i32 s6, 2
	v_readlane_b32 s5, v235, 10
	s_cselect_b64 s[2:3], -1, 0
	s_cmp_lt_i32 s7, 3
	s_cselect_b64 s[4:5], -1, 0
	s_or_b64 s[2:3], s[2:3], s[4:5]
	s_and_b64 vcc, exec, s[2:3]
	s_cbranch_vccnz .LBB0_194
	s_cmpk_lt_i32 s50, 0xd0
	v_readlane_b32 s4, v235, 57
	s_cselect_b64 s[2:3], -1, 0
	s_cmp_lg_u32 s4, 0
	s_cselect_b64 s[4:5], -1, 0
	s_or_b64 s[2:3], s[2:3], s[4:5]
	s_add_i32 s6, s50, 0xffffff93
	s_and_b64 s[4:5], s[2:3], exec
	s_cselect_b32 s28, s50, s6
	s_cmp_lt_i32 s92, s28
	s_cselect_b64 s[4:5], -1, 0
	s_or_b64 s[4:5], s[2:3], s[4:5]
	s_mov_b64 s[2:3], -1
	s_and_b64 vcc, exec, s[4:5]
	s_cbranch_vccnz .LBB0_169
	s_sub_i32 s2, s92, s28
	s_lshl_b32 s2, s2, 3
	v_readlane_b32 s3, v235, 52
	s_add_i32 s2, s2, s3
	s_cmpk_gt_u32 s2, 0x439f
	s_barrier
	s_cbranch_scc1 .LBB0_168
	v_readlane_b32 s4, v235, 9
	v_readlane_b32 s5, v235, 10
	s_add_u32 s20, s4, 0x1600000
	s_addc_u32 s21, s5, 0
	s_add_u32 s22, s4, 0x17600000
	s_addc_u32 s23, s5, 0
	s_and_b32 s3, s2, 0xffff
	s_mul_i32 s3, s3, 0xf83f
	s_lshr_b32 s5, s3, 26
	s_mul_i32 s3, s5, 0x420
	v_readlane_b32 s7, v235, 12
	s_sub_i32 s2, s2, s3
	s_and_b32 s7, s2, 0xffff
	s_mul_i32 s3, s7, 0xba2f
	s_lshr_b32 s3, s3, 24
	s_mulk_i32 s3, 0x160
	s_sub_i32 s12, s2, s3
	s_cmpk_gt_u32 s7, 0x2bf
	v_readlane_b32 s6, v235, 11
	s_cbranch_scc0 .LBB0_141
	s_and_b32 s3, 0xffff, s5
	v_readlane_b32 s36, v235, 0
	s_and_b32 s2, 0xffff, s12
	s_mul_i32 s4, s3, 0xb00000
	v_readlane_b32 s38, v235, 2
	v_readlane_b32 s39, v235, 3
	s_add_u32 s8, s38, s4
	s_addc_u32 s9, s39, 0
	s_lshl_b32 s4, s2, 3
	s_lshl_b32 s2, s2, 6
	s_and_b32 s6, s4, 0xf80
	s_and_b32 s4, s2, 0x3c0
	s_mul_i32 s3, s3, 0x2c0000
	s_add_u32 s10, s22, s3
	v_readlane_b32 s37, v235, 1
	v_readlane_b32 s40, v235, 4
	v_readlane_b32 s41, v235, 5
	v_readlane_b32 s42, v235, 6
	v_readlane_b32 s43, v235, 7
	s_addc_u32 s11, s23, 0
	s_cbranch_execz .LBB0_142
	v_mov_b32_e32 v130, s4
	s_movk_i32 s24, 0xb00
	s_movk_i32 s18, 0x400
	s_branch .LBB0_143

; #define LAS __attribute__((address_space(3)))
; DI void phase_p0(const Args& A, LAS unsigned char* lds, int it0, int it1, int gw, int ngw, int wave, int lane) {
;     ...
;     auto desc = [&](int item) { F8Tile d; const int r = item - I_IN - I_OUT; const int le = r / (3 * I_E), q = r % (3 * I_E), which = q / I_E, t = q % I_E;
;         if (which < 2) { const int kb = t / 44, nb = t % 44, n0 = nb * 64;
;             d.W = A.in[which == 0 ? I_EW1 : I_EW3] + (size_t)le * DM * FF; d.N = FF; d.k0 = kb * 128; d.n0 = n0; d.dst = w13 + (size_t)le * 5632 * DM; d.Kd = DM; d.drow0 = (size_t)((n0 >> 7) * 256 + which * 128 + (n0 & 127)); }
;         else { const int kb = t / 16, nb = t % 16;
;             d.W = A.in[I_EW2] + (size_t)le * FF * DM; d.N = DM; d.k0 = kb * 128; d.n0 = nb * 64; d.dst = w2t + (size_t)le * DM * FF; d.Kd = FF; d.drow0 = (size_t)nb * 64; }
;         return d; };
;     if (it < it1) {
;         f32x4 ra[4][4], rb[4][4]; LAS unsigned char* sc8 = (LAS unsigned char*)scr;
;         F8Tile d = desc(it);
;         f8_load(ra, d, 0, lane); f8_load(rb, d, 1, lane);
;         for (; it < it1; it += ngw) {
;             const bool vn = it + ngw < it1; F8Tile dn = d; if (vn) dn = desc(it + ngw);
;             f8_convert_reload(ra, 0, F8_WSC, sc8, vn, dn, lane);
;             f8_convert_reload(rb, 1, F8_WSC, sc8, vn, dn, lane);
;             f8_store(d, sc8, lane);
;             d = dn;
.LBB0_145:
	s_add_i32 s26, s2, 0x368
	s_cmpk_lt_i32 s26, 0x4a60
	s_cselect_b64 s[16:17], -1, 0
	s_cmpk_gt_i32 s26, 0x4a5f
	s_cselect_b64 s[14:15], -1, 0
	s_and_b64 vcc, exec, s[14:15]
	s_mov_b32 s27, s6
	s_cbranch_vccnz .LBB0_152
	s_addk_i32 s2, 0xfca8
	s_mul_hi_i32 s3, s2, 0x3e0f83e1
	s_lshr_b32 s4, s3, 31
	s_ashr_i32 s7, s3, 8
	s_add_i32 s7, s7, s4
	s_mul_i32 s3, s7, 0x420
	s_sub_i32 s29, s2, s3
	s_mul_i32 s2, s29, 0xba3
	s_lshr_b32 s3, s2, 31
	s_ashr_i32 s34, s2, 20
	s_add_i32 s34, s34, s3
	s_mul_i32 s2, s34, 0x160
	s_sub_i32 s33, s29, s2
	s_mov_b64 s[18:19], -1
	s_cmpk_gt_i32 s29, 0x2bf
	s_sext_i32_i16 s35, s33
	s_mul_hi_i32 s30, s7, 0xb00000
	s_mul_i32 s31, s7, 0xb00000
	s_cbranch_scc0 .LBB0_148
	v_readlane_b32 s36, v235, 0
	v_readlane_b32 s38, v235, 2
	v_readlane_b32 s39, v235, 3
	s_add_u32 s8, s38, s31
	s_addc_u32 s9, s39, s30
	s_lshl_b32 s2, s35, 3
	s_and_b32 s27, s2, 0xf80
	s_lshl_b32 s2, s35, 6
	s_and_b32 s4, s2, 0x3c0
	s_mul_i32 s3, s7, 0x2c0000
	s_mul_hi_i32 s2, s7, 0x2c0000
	s_add_u32 s12, s22, s3
	v_readlane_b32 s37, v235, 1
	v_readlane_b32 s40, v235, 4
	v_readlane_b32 s41, v235, 5
	v_readlane_b32 s42, v235, 6
	v_readlane_b32 s43, v235, 7
	s_addc_u32 s13, s23, s2
	s_mov_b64 s[18:19], 0
	s_mov_b64 s[2:3], s[4:5]

; #define LAS __attribute__((address_space(3)))
; #define PH(k, ...) do { if (IN(pb + (k))) { { __VA_ARGS__ } if ((MK_DUP >> (k)) & 1) { xcd_barrier(bar); { __VA_ARGS__ } } } SEAM(pb + (k)); } while (0)
; DI void phase_p0(const Args& A, LAS unsigned char* lds, int it0, int it1, int gw, int ngw, int wave, int lane) {
;     ...
;     auto desc = [&](int item) { F8Tile d; const int r = item - I_IN - I_OUT; const int le = r / (3 * I_E), q = r % (3 * I_E), which = q / I_E, t = q % I_E;
;         if (which < 2) { const int kb = t / 44, nb = t % 44, n0 = nb * 64;
;             d.W = A.in[which == 0 ? I_EW1 : I_EW3] + (size_t)le * DM * FF; d.N = FF; d.k0 = kb * 128; d.n0 = n0; d.dst = w13 + (size_t)le * 5632 * DM; d.Kd = DM; d.drow0 = (size_t)((n0 >> 7) * 256 + which * 128 + (n0 & 127)); }
;         else { const int kb = t / 16, nb = t % 16;
;             d.W = A.in[I_EW2] + (size_t)le * FF * DM; d.N = DM; d.k0 = kb * 128; d.n0 = nb * 64; d.dst = w2t + (size_t)le * DM * FF; d.Kd = FF; d.drow0 = (size_t)nb * 64; }
;         return d; };
;     if (it < it1) {
;         f32x4 ra[4][4], rb[4][4]; LAS unsigned char* sc8 = (LAS unsigned char*)scr;
;         F8Tile d = desc(it);
;         f8_load(ra, d, 0, lane); f8_load(rb, d, 1, lane);
;         for (; it < it1; it += ngw) {
;             const bool vn = it + ngw < it1; F8Tile dn = d; if (vn) dn = desc(it + ngw);
; template <int l> DI void run_layer(const Args& A, LAS unsigned char* lds, const XcdBarrier& bar, int lo, int hi, int G, int bid, int tid, int lane, int wave, int gw, int ngw, int gtid, int nthr) {
;     ...
;     PH(8,
;         const bool conv = (l == 0) && (P0_SPLIT < P0_END) && (G >= 2 * P0_XC) && (G % 8 == 0); const int Gg = conv ? G - P0_XC : G;
;         if (conv && bid >= Gg) { __syncthreads(); phase_p0(A, lds, P0_SPLIT, P0_END, (bid - Gg) * NWAVES + wave, P0_XC * NWAVES, wave, lane); __syncthreads(); }
.LBB0_1337:
	s_cmp_lt_i32 s6, 10
	s_cselect_b64 s[8:9], -1, 0
	s_and_b64 s[0:1], s[8:9], s[0:1]
	s_andn2_b64 vcc, exec, s[0:1]
	s_cbranch_vccnz .LBB0_1395
	s_cmpk_lt_i32 s50, 0xa0
	v_readlane_b32 s2, v235, 57
	s_cselect_b64 s[0:1], -1, 0
	s_cmp_lg_u32 s2, 0
	s_cselect_b64 s[2:3], -1, 0
	s_or_b64 s[0:1], s[0:1], s[2:3]
	s_add_i32 s4, s50, 0xffffffb0
	s_and_b64 s[2:3], s[0:1], exec
	s_cselect_b32 s30, s50, s4
	s_cmp_lt_i32 s92, s30
	s_cselect_b64 s[2:3], -1, 0
	s_or_b64 s[2:3], s[0:1], s[2:3]
	s_mov_b64 s[0:1], -1
	s_and_b64 vcc, exec, s[2:3]
	s_cbranch_vccnz .LBB0_1371
	s_sub_i32 s0, s92, s30
	s_lshl_b32 s0, s0, 3
	v_readlane_b32 s1, v235, 52
	s_add_i32 s0, s0, s1
	s_cmpk_gt_u32 s0, 0x405f
	s_waitcnt vmcnt(0)
	s_barrier
	s_cbranch_scc1 .LBB0_1370
	v_readlane_b32 s4, v235, 9
	v_readlane_b32 s5, v235, 10
	s_add_u32 s18, s4, 0x1600000
	s_addc_u32 s19, s5, 0
	s_add_u32 s20, s4, 0x17600000
	s_addc_u32 s21, s5, 0
	s_addk_i32 s0, 0x43a0
	s_and_b32 s1, s0, 0xffff
	s_mul_i32 s1, s1, 0xf83f
	s_lshr_b32 s1, s1, 26
	s_mul_i32 s2, s1, 0x420
	s_sub_i32 s0, s0, s2
	s_and_b32 s5, s0, 0xffff
	s_mul_i32 s2, s5, 0xba2f
	s_lshr_b32 s2, s2, 24
	s_mulk_i32 s2, 0x160
	s_sub_i32 s12, s0, s2
	s_cmpk_gt_u32 s5, 0x2bf
	v_readlane_b32 s6, v235, 11
	v_readlane_b32 s7, v235, 12
	s_cbranch_scc0 .LBB0_1343
	s_and_b32 s2, 0xffff, s1
	v_readlane_b32 s36, v235, 0
	s_and_b32 s0, 0xffff, s12
	s_mul_i32 s3, s2, 0xb00000
	v_readlane_b32 s38, v235, 2
	v_readlane_b32 s39, v235, 3
	s_add_u32 s6, s38, s3
	s_addc_u32 s7, s39, 0
	s_lshl_b32 s3, s0, 3
	s_lshl_b32 s0, s0, 6
	s_and_b32 s4, s3, 0xf80
	s_and_b32 s0, s0, 0x3c0
	s_mul_i32 s2, s2, 0x2c0000
	s_add_u32 s10, s20, s2
	v_readlane_b32 s37, v235, 1
	v_readlane_b32 s40, v235, 4
	v_readlane_b32 s41, v235, 5
	v_readlane_b32 s42, v235, 6
	v_readlane_b32 s43, v235, 7
	s_addc_u32 s11, s21, 0
	s_cbranch_execz .LBB0_1344
	v_mov_b32_e32 v130, s0
	s_movk_i32 s22, 0xb00
	s_movk_i32 s16, 0x400
	s_branch .LBB0_1345

; DI void f8_load(f32x4 (&v)[4][4], const F8Tile& d, int hb, int lane) {
;     const int nq = lane & 15, kq = lane >> 4;
; #pragma unroll
;     for (int it = 0; it < 4; ++it)
; #pragma unroll
;         for (int j = 0; j < 4; ++j) v[it][j] = __builtin_nontemporal_load((const f32x4*)(d.W + (size_t)(d.k0 + hb * 64 + it * 16 + kq * 4 + j) * d.N + d.n0 + 4 * nq));
; }
.LBB0_1345:
	v_lshrrev_b32_e32 v2, 2, v146
	v_and_b32_e32 v1, 12, v2
	v_or_b32_e32 v187, 0x72, v1
	v_or_b32_e32 v188, 0x73, v2
	v_mov_b32_e32 v135, 0
	v_or_b32_e32 v159, 3, v2
	v_or_b32_e32 v163, 19, v2
	v_or_b32_e32 v167, 35, v2
	v_or_b32_e32 v172, 51, v2
	v_or_b32_e32 v176, 0x43, v2
	v_or_b32_e32 v180, 0x53, v2
	v_or_b32_e32 v184, 0x63, v2
	v_add_u32_e32 v2, s4, v188
	v_add_u32_e32 v4, s4, v187
	s_mov_b32 s1, 0
	v_lshlrev_b32_e32 v3, 2, v0
	v_mul_u32_u24_e32 v134, s16, v2
	v_mul_u32_u24_e32 v4, s16, v4
	v_mov_b32_e32 v5, v135
	v_and_b32_e32 v132, 60, v3
	v_lshl_add_u64 v[2:3], v[134:135], 2, s[6:7]
	s_lshl_b64 s[2:3], s[0:1], 2
	v_lshl_add_u64 v[4:5], v[4:5], 2, s[6:7]
	v_lshl_add_u64 v[2:3], v[2:3], 0, s[2:3]
	v_lshlrev_b32_e32 v134, 2, v132
	v_lshl_add_u64 v[4:5], v[4:5], 0, s[2:3]
	v_or_b32_e32 v183, 0x62, v1
	v_or_b32_e32 v185, 0x70, v1
	v_or_b32_e32 v186, 0x71, v1
	v_lshl_add_u64 v[2:3], v[2:3], 0, v[134:135]
	v_lshl_add_u64 v[4:5], v[4:5], 0, v[134:135]
	global_load_dwordx4 v[10:13], v[2:3], off nt
	global_load_dwordx4 v[14:17], v[4:5], off nt
	v_add_u32_e32 v2, s4, v186
	v_add_u32_e32 v4, s4, v185
	v_add_u32_e32 v18, s4, v184
	v_add_u32_e32 v20, s4, v183
	v_mul_u32_u24_e32 v2, s16, v2
	v_mov_b32_e32 v3, v135
	v_mul_u32_u24_e32 v4, s16, v4
	v_mov_b32_e32 v5, v135
	v_mul_u32_u24_e32 v18, s16, v18
	v_mov_b32_e32 v19, v135
	v_mul_u32_u24_e32 v20, s16, v20
	v_mov_b32_e32 v21, v135
	v_lshl_add_u64 v[2:3], v[2:3], 2, s[6:7]
	v_lshl_add_u64 v[4:5], v[4:5], 2, s[6:7]
	v_lshl_add_u64 v[18:19], v[18:19], 2, s[6:7]
	v_lshl_add_u64 v[20:21], v[20:21], 2, s[6:7]
	v_lshl_add_u64 v[2:3], v[2:3], 0, s[2:3]
	v_lshl_add_u64 v[4:5], v[4:5], 0, s[2:3]
	v_lshl_add_u64 v[18:19], v[18:19], 0, s[2:3]
	v_lshl_add_u64 v[20:21], v[20:21], 0, s[2:3]
	v_or_b32_e32 v179, 0x52, v1
	v_or_b32_e32 v181, 0x60, v1
	v_or_b32_e32 v182, 0x61, v1
	v_lshl_add_u64 v[2:3], v[2:3], 0, v[134:135]
	v_lshl_add_u64 v[6:7], v[4:5], 0, v[134:135]
	v_lshl_add_u64 v[18:19], v[18:19], 0, v[134:135]
	v_lshl_add_u64 v[20:21], v[20:21], 0, v[134:135]
	global_load_dwordx4 v[2:5], v[2:3], off nt
	s_nop 0
	global_load_dwordx4 v[6:9], v[6:7], off nt
	s_nop 0
	global_load_dwordx4 v[26:29], v[18:19], off nt
	global_load_dwordx4 v[30:33], v[20:21], off nt
	v_add_u32_e32 v18, s4, v182
	v_add_u32_e32 v20, s4, v181
	v_add_u32_e32 v34, s4, v180
	v_add_u32_e32 v36, s4, v179
	v_mul_u32_u24_e32 v18, s16, v18
	v_mov_b32_e32 v19, v135
	v_mul_u32_u24_e32 v20, s16, v20
	v_mov_b32_e32 v21, v135
	v_mul_u32_u24_e32 v34, s16, v34
	v_mov_b32_e32 v35, v135
	v_mul_u32_u24_e32 v36, s16, v36
	v_mov_b32_e32 v37, v135
	v_lshl_add_u64 v[18:19], v[18:19], 2, s[6:7]
	v_lshl_add_u64 v[20:21], v[20:21], 2, s[6:7]
	v_lshl_add_u64 v[34:35], v[34:35], 2, s[6:7]
	v_lshl_add_u64 v[36:37], v[36:37], 2, s[6:7]
	v_lshl_add_u64 v[18:19], v[18:19], 0, s[2:3]
	v_lshl_add_u64 v[20:21], v[20:21], 0, s[2:3]
	v_lshl_add_u64 v[34:35], v[34:35], 0, s[2:3]
	v_lshl_add_u64 v[36:37], v[36:37], 0, s[2:3]
	v_or_b32_e32 v175, 0x42, v1
	v_or_b32_e32 v177, 0x50, v1
	v_or_b32_e32 v178, 0x51, v1
	v_lshl_add_u64 v[18:19], v[18:19], 0, v[134:135]
	v_lshl_add_u64 v[22:23], v[20:21], 0, v[134:135]
	v_lshl_add_u64 v[34:35], v[34:35], 0, v[134:135]
	v_lshl_add_u64 v[36:37], v[36:37], 0, v[134:135]
	global_load_dwordx4 v[18:21], v[18:19], off nt
	s_nop 0
	global_load_dwordx4 v[22:25], v[22:23], off nt
	s_nop 0
	global_load_dwordx4 v[42:45], v[34:35], off nt
	global_load_dwordx4 v[46:49], v[36:37], off nt
	v_add_u32_e32 v34, s4, v178
	v_add_u32_e32 v36, s4, v177
	v_add_u32_e32 v50, s4, v176
	v_add_u32_e32 v52, s4, v175
	v_mul_u32_u24_e32 v34, s16, v34
	v_mov_b32_e32 v35, v135
	v_mul_u32_u24_e32 v36, s16, v36
	v_mov_b32_e32 v37, v135
	v_mul_u32_u24_e32 v50, s16, v50
	v_mov_b32_e32 v51, v135
	v_mul_u32_u24_e32 v52, s16, v52
	v_mov_b32_e32 v53, v135
	v_lshl_add_u64 v[34:35], v[34:35], 2, s[6:7]
	v_lshl_add_u64 v[36:37], v[36:37], 2, s[6:7]
	v_lshl_add_u64 v[50:51], v[50:51], 2, s[6:7]
	v_lshl_add_u64 v[52:53], v[52:53], 2, s[6:7]
	v_lshl_add_u64 v[34:35], v[34:35], 0, s[2:3]
	v_lshl_add_u64 v[36:37], v[36:37], 0, s[2:3]
	v_lshl_add_u64 v[50:51], v[50:51], 0, s[2:3]
	v_lshl_add_u64 v[52:53], v[52:53], 0, s[2:3]
	v_or_b32_e32 v171, 50, v1
	v_or_b32_e32 v173, 64, v1
	v_or_b32_e32 v174, 0x41, v1
	v_lshl_add_u64 v[34:35], v[34:35], 0, v[134:135]
	v_lshl_add_u64 v[38:39], v[36:37], 0, v[134:135]
	v_lshl_add_u64 v[50:51], v[50:51], 0, v[134:135]
	v_lshl_add_u64 v[52:53], v[52:53], 0, v[134:135]
	global_load_dwordx4 v[34:37], v[34:35], off nt
	s_nop 0
	global_load_dwordx4 v[38:41], v[38:39], off nt
	s_nop 0
	global_load_dwordx4 v[58:61], v[50:51], off nt
	global_load_dwordx4 v[62:65], v[52:53], off nt
	v_add_u32_e32 v50, s4, v174
	v_add_u32_e32 v52, s4, v173
	v_add_u32_e32 v66, s4, v172
	v_add_u32_e32 v68, s4, v171
	v_mul_u32_u24_e32 v50, s16, v50
	v_mov_b32_e32 v51, v135
	v_mul_u32_u24_e32 v52, s16, v52
	v_mov_b32_e32 v53, v135
	v_mul_u32_u24_e32 v66, s16, v66
	v_mov_b32_e32 v67, v135
	v_mul_u32_u24_e32 v68, s16, v68
	v_mov_b32_e32 v69, v135
	v_lshl_add_u64 v[50:51], v[50:51], 2, s[6:7]
	v_lshl_add_u64 v[52:53], v[52:53], 2, s[6:7]
	v_lshl_add_u64 v[66:67], v[66:67], 2, s[6:7]
	v_lshl_add_u64 v[68:69], v[68:69], 2, s[6:7]
	v_lshl_add_u64 v[50:51], v[50:51], 0, s[2:3]
	v_lshl_add_u64 v[52:53], v[52:53], 0, s[2:3]
	v_lshl_add_u64 v[66:67], v[66:67], 0, s[2:3]
	v_lshl_add_u64 v[68:69], v[68:69], 0, s[2:3]
	v_or_b32_e32 v166, 34, v1
	v_or_b32_e32 v168, 48, v1
	v_or_b32_e32 v169, 49, v1
	v_lshl_add_u64 v[50:51], v[50:51], 0, v[134:135]
	v_lshl_add_u64 v[54:55], v[52:53], 0, v[134:135]
	v_lshl_add_u64 v[66:67], v[66:67], 0, v[134:135]
; #define LAS __attribute__((address_space(3)))
; DI unsigned pk4_fp8(float a, float b, float c, float d) { unsigned p = 0u; p = __builtin_amdgcn_cvt_pk_fp8_f32(f8clamp(a), f8clamp(b), p, false); p = __builtin_amdgcn_cvt_pk_fp8_f32(f8clamp(c), f8clamp(d), p, true); return p; }
; DI void f8_load(f32x4 (&v)[4][4], const F8Tile& d, int hb, int lane) {
;     const int nq = lane & 15, kq = lane >> 4;
; #pragma unroll
;     for (int it = 0; it < 4; ++it)
; #pragma unroll
;         for (int j = 0; j < 4; ++j) v[it][j] = __builtin_nontemporal_load((const f32x4*)(d.W + (size_t)(d.k0 + hb * 64 + it * 16 + kq * 4 + j) * d.N + d.n0 + 4 * nq));
; }
; DI void f8_convert(const f32x4 (&v)[4][4], int hb, float sc, LAS unsigned char* scr, int lane) {
;     const int nq = lane & 15, kq = lane >> 4;
; #pragma unroll
;     for (int it = 0; it < 4; ++it)
; #pragma unroll
;         for (int i = 0; i < 4; ++i) *(LAS unsigned*)(scr + (4 * nq + i) * 132 + hb * 64 + it * 16 + kq * 4) = pk4_fp8(v[it][0][i] * sc, v[it][1][i] * sc, v[it][2][i] * sc, v[it][3][i] * sc);
; }
; DI void phase_p0(const Args& A, LAS unsigned char* lds, int it0, int it1, int gw, int ngw, int wave, int lane) {
;     ...
;     auto desc = [&](int item) { F8Tile d; const int r = item - I_IN - I_OUT; const int le = r / (3 * I_E), q = r % (3 * I_E), which = q / I_E, t = q % I_E;
;         if (which < 2) { const int kb = t / 44, nb = t % 44, n0 = nb * 64;
;             d.W = A.in[which == 0 ? I_EW1 : I_EW3] + (size_t)le * DM * FF; d.N = FF; d.k0 = kb * 128; d.n0 = n0; d.dst = w13 + (size_t)le * 5632 * DM; d.Kd = DM; d.drow0 = (size_t)((n0 >> 7) * 256 + which * 128 + (n0 & 127)); }
;         else { const int kb = t / 16, nb = t % 16;
;             d.W = A.in[I_EW2] + (size_t)le * FF * DM; d.N = DM; d.k0 = kb * 128; d.n0 = nb * 64; d.dst = w2t + (size_t)le * DM * FF; d.Kd = FF; d.drow0 = (size_t)nb * 64; }
;         return d; };
;     if (it < it1) {
;         f32x4 ra[4][4], rb[4][4]; LAS unsigned char* sc8 = (LAS unsigned char*)scr;
;         F8Tile d = desc(it);
;         f8_load(ra, d, 0, lane); f8_load(rb, d, 1, lane);
;         for (; it < it1; it += ngw) {
;             const bool vn = it + ngw < it1; F8Tile dn = d; if (vn) dn = desc(it + ngw);
	v_lshl_add_u64 v[68:69], v[68:69], 0, v[134:135]
	global_load_dwordx4 v[50:53], v[50:51], off nt
	s_nop 0
	global_load_dwordx4 v[54:57], v[54:55], off nt
	s_nop 0
	global_load_dwordx4 v[78:81], v[66:67], off nt
	global_load_dwordx4 v[74:77], v[68:69], off nt
	v_add_u32_e32 v66, s4, v169
	v_add_u32_e32 v68, s4, v168
	v_add_u32_e32 v82, s4, v167
	v_add_u32_e32 v84, s4, v166
	v_mul_u32_u24_e32 v66, s16, v66
	v_mov_b32_e32 v67, v135
	v_mul_u32_u24_e32 v68, s16, v68
	v_mov_b32_e32 v69, v135
	v_mul_u32_u24_e32 v82, s16, v82
	v_mov_b32_e32 v83, v135
	v_mul_u32_u24_e32 v84, s16, v84
	v_mov_b32_e32 v85, v135
	v_lshl_add_u64 v[66:67], v[66:67], 2, s[6:7]
	v_lshl_add_u64 v[68:69], v[68:69], 2, s[6:7]
	v_lshl_add_u64 v[82:83], v[82:83], 2, s[6:7]
	v_lshl_add_u64 v[84:85], v[84:85], 2, s[6:7]
	v_lshl_add_u64 v[66:67], v[66:67], 0, s[2:3]
	v_lshl_add_u64 v[68:69], v[68:69], 0, s[2:3]
	v_lshl_add_u64 v[82:83], v[82:83], 0, s[2:3]
	v_lshl_add_u64 v[84:85], v[84:85], 0, s[2:3]
	v_or_b32_e32 v162, 18, v1
	v_or_b32_e32 v164, 32, v1
	v_or_b32_e32 v165, 33, v1
	v_lshl_add_u64 v[66:67], v[66:67], 0, v[134:135]
	v_lshl_add_u64 v[70:71], v[68:69], 0, v[134:135]
	v_lshl_add_u64 v[82:83], v[82:83], 0, v[134:135]
	v_lshl_add_u64 v[84:85], v[84:85], 0, v[134:135]
	global_load_dwordx4 v[66:69], v[66:67], off nt
	s_nop 0
	global_load_dwordx4 v[70:73], v[70:71], off nt
	s_nop 0
	global_load_dwordx4 v[90:93], v[82:83], off nt
	global_load_dwordx4 v[94:97], v[84:85], off nt
	v_add_u32_e32 v82, s4, v165
	v_add_u32_e32 v84, s4, v164
	v_add_u32_e32 v98, s4, v163
	v_add_u32_e32 v100, s4, v162
	v_mul_u32_u24_e32 v82, s16, v82
	v_mov_b32_e32 v83, v135
	v_mul_u32_u24_e32 v84, s16, v84
	v_mov_b32_e32 v85, v135
	v_mul_u32_u24_e32 v98, s16, v98
	v_mov_b32_e32 v99, v135
	v_mul_u32_u24_e32 v100, s16, v100
	v_mov_b32_e32 v101, v135
	v_lshl_add_u64 v[82:83], v[82:83], 2, s[6:7]
	v_lshl_add_u64 v[84:85], v[84:85], 2, s[6:7]
	v_lshl_add_u64 v[98:99], v[98:99], 2, s[6:7]
	v_lshl_add_u64 v[100:101], v[100:101], 2, s[6:7]
	v_lshl_add_u64 v[82:83], v[82:83], 0, s[2:3]
	v_lshl_add_u64 v[84:85], v[84:85], 0, s[2:3]
	v_lshl_add_u64 v[98:99], v[98:99], 0, s[2:3]
	v_lshl_add_u64 v[100:101], v[100:101], 0, s[2:3]
	v_or_b32_e32 v158, 2, v1
	v_or_b32_e32 v160, 16, v1
	v_or_b32_e32 v161, 17, v1
	v_lshl_add_u64 v[82:83], v[82:83], 0, v[134:135]
	v_lshl_add_u64 v[86:87], v[84:85], 0, v[134:135]
	v_lshl_add_u64 v[98:99], v[98:99], 0, v[134:135]
	v_lshl_add_u64 v[100:101], v[100:101], 0, v[134:135]
	global_load_dwordx4 v[82:85], v[82:83], off nt
	s_nop 0
	global_load_dwordx4 v[86:89], v[86:87], off nt
	s_nop 0
	global_load_dwordx4 v[106:109], v[98:99], off nt
	global_load_dwordx4 v[110:113], v[100:101], off nt
	v_add_u32_e32 v98, s4, v161
	v_add_u32_e32 v100, s4, v160
	v_add_u32_e32 v114, s4, v159
	v_add_u32_e32 v116, s4, v158
	v_mul_u32_u24_e32 v98, s16, v98
	v_mov_b32_e32 v99, v135
	v_mul_u32_u24_e32 v100, s16, v100
	v_mov_b32_e32 v101, v135
	v_mul_u32_u24_e32 v114, s16, v114
	v_mov_b32_e32 v115, v135
	v_mul_u32_u24_e32 v116, s16, v116
	v_mov_b32_e32 v117, v135
	v_lshl_add_u64 v[98:99], v[98:99], 2, s[6:7]
	v_lshl_add_u64 v[100:101], v[100:101], 2, s[6:7]
	v_lshl_add_u64 v[114:115], v[114:115], 2, s[6:7]
	v_lshl_add_u64 v[116:117], v[116:117], 2, s[6:7]
	v_lshl_add_u64 v[98:99], v[98:99], 0, s[2:3]
	v_lshl_add_u64 v[100:101], v[100:101], 0, s[2:3]
	v_lshl_add_u64 v[114:115], v[114:115], 0, s[2:3]
	v_lshl_add_u64 v[116:117], v[116:117], 0, s[2:3]
	v_or_b32_e32 v133, 1, v1
	v_lshl_add_u64 v[98:99], v[98:99], 0, v[134:135]
	v_lshl_add_u64 v[102:103], v[100:101], 0, v[134:135]
	v_lshl_add_u64 v[114:115], v[114:115], 0, v[134:135]
	v_lshl_add_u64 v[116:117], v[116:117], 0, v[134:135]
	global_load_dwordx4 v[98:101], v[98:99], off nt
	s_nop 0
	global_load_dwordx4 v[102:105], v[102:103], off nt
	s_nop 0
	global_load_dwordx4 v[122:125], v[114:115], off nt
	global_load_dwordx4 v[126:129], v[116:117], off nt
	v_add_u32_e32 v114, s4, v133
	v_add_u32_e32 v116, s4, v1
	v_mul_u32_u24_e32 v114, s16, v114
	v_mov_b32_e32 v115, v135
	v_mul_u32_u24_e32 v116, s16, v116
	v_mov_b32_e32 v117, v135
	v_lshl_add_u64 v[114:115], v[114:115], 2, s[6:7]
	v_lshl_add_u64 v[116:117], v[116:117], 2, s[6:7]
	v_lshl_add_u64 v[114:115], v[114:115], 0, s[2:3]
	v_lshl_add_u64 v[116:117], v[116:117], 0, s[2:3]
	v_lshl_add_u64 v[114:115], v[114:115], 0, v[134:135]
	v_lshl_add_u64 v[118:119], v[116:117], 0, v[134:135]
	global_load_dwordx4 v[114:117], v[114:115], off nt
	s_nop 0
	global_load_dwordx4 v[118:121], v[118:119], off nt
	v_readlane_b32 s2, v235, 52
	s_mulk_i32 s2, 0x4200
	v_lshlrev_b32_e32 v137, 4, v0
	s_add_i32 s2, s2, 0
	v_and_b32_e32 v138, 0x70, v137
	v_add_u32_e32 v134, s2, v1
	v_lshrrev_b32_e32 v136, 3, v146
	v_add_u32_e32 v157, s2, v138
	s_lshl_b32 s2, s30, 3
	v_readlane_b32 s12, v235, 54
	v_mov_b32_e32 v131, v135
	v_mul_u32_u24_e32 v156, 0x84, v132
	v_mul_u32_u24_e32 v189, 0x84, v136
	v_readlane_b32 s13, v235, 55
	s_sub_i32 s2, s12, s2
	v_mov_b32_e32 v139, v135
	v_mov_b32_e32 v137, v135
	v_or_b32_e32 v140, 8, v136
	v_mov_b32_e32 v141, v135
	v_or_b32_e32 v142, 16, v136
	v_mov_b32_e32 v143, v135
	v_or_b32_e32 v144, 24, v136
	v_mov_b32_e32 v145, v135
	v_or_b32_e32 v148, 32, v136
	v_mov_b32_e32 v149, v135
	v_or_b32_e32 v150, 40, v136
	v_mov_b32_e32 v151, v135
	v_or_b32_e32 v152, 48, v136
	v_mov_b32_e32 v153, v135
	v_or_b32_e32 v154, 56, v136
	v_mov_b32_e32 v155, v135
	s_add_i32 s23, s2, 0x4620
	s_mov_b32 s24, 0xc3e00000
	v_add_u32_e32 v189, v157, v189
	v_mov_b32_e32 v190, 0x43e00000
	v_add_u32_e32 v191, v134, v156
	v_mov_b64_e32 v[156:157], v[130:131]
	s_mov_b32 s17, s22
	s_mov_b64 s[12:13], s[10:11]
	s_waitcnt vmcnt(0)
	s_branch .LBB0_1347
